# baseline (speedup 1.0000x reference)
.Ls1_am:
	s_sub_u32 s59, s49, 1
	s_waitcnt vmcnt(16)
	v_cvt_pk_f16_f32 v228, v228, v229
	v_cvt_pk_f16_f32 v229, v230, v231
	v_cvt_pk_f16_f32 v230, v232, v233
	v_cvt_pk_f16_f32 v231, v234, v235
	s_cmp_lt_u32 s59, 4
	s_cselect_b32 s52, s62, s64
	s_cselect_b32 s53, s63, s65
	s_and_b32 s58, s59, 3
	s_lshl_b32 s58, s58, 15
	s_add_u32 s52, s52, s58
	s_addc_u32 s53, s53, 0
	global_store_dwordx4 v237, v[228:231], s[52:53] sc1 nt
	s_add_u32 s59, s59, 1
	s_cmp_lt_u32 s59, 4
	s_cselect_b32 s52, s68, s70
	s_cselect_b32 s53, s69, s71
	s_and_b32 s58, s59, 3
	s_lshl_b32 s58, s58, 16
	s_add_u32 s52, s52, s58
	s_addc_u32 s53, s53, 0
	global_load_dwordx4 v[228:231], v236, s[52:53] nt
	global_load_dwordx4 v[232:235], v236, s[52:53] offset:16 nt
	s_waitcnt vmcnt(9)
	s_branch .Ls1_join
.Ls1_al:
	s_mov_b32 s59, 7
	s_waitcnt vmcnt(16)
	v_cvt_pk_f16_f32 v228, v228, v229
	v_cvt_pk_f16_f32 v229, v230, v231
	v_cvt_pk_f16_f32 v230, v232, v233
	v_cvt_pk_f16_f32 v231, v234, v235
	s_cmp_lt_u32 s59, 4
	s_cselect_b32 s52, s62, s64
	s_cselect_b32 s53, s63, s65
	s_and_b32 s58, s59, 3
	s_lshl_b32 s58, s58, 15
	s_add_u32 s52, s52, s58
	s_addc_u32 s53, s53, 0
	global_store_dwordx4 v237, v[228:231], s[52:53] sc1 nt
	s_waitcnt vmcnt(7)
	s_branch .Ls1_join

.Ls1_bm:
	s_sub_u32 s59, s49, 10
	s_waitcnt vmcnt(16)
	v_cvt_pk_f16_f32 v228, v228, v229
	v_cvt_pk_f16_f32 v229, v230, v231
	v_cvt_pk_f16_f32 v230, v232, v233
	v_cvt_pk_f16_f32 v231, v234, v235
	s_cmp_lt_u32 s59, 4
	s_cselect_b32 s52, s62, s64
	s_cselect_b32 s53, s63, s65
	s_and_b32 s58, s59, 3
	s_lshl_b32 s58, s58, 15
	s_add_u32 s58, s58, 0x800
	s_add_u32 s52, s52, s58
	s_addc_u32 s53, s53, 0
	global_store_dwordx4 v237, v[228:231], s[52:53] sc1 nt
	s_add_u32 s59, s59, 1
	s_cmp_lt_u32 s59, 4
	s_cselect_b32 s52, s68, s70
	s_cselect_b32 s53, s69, s71
	s_and_b32 s58, s59, 3
	s_lshl_b32 s58, s58, 16
	s_add_u32 s58, s58, 0x1000
	s_add_u32 s52, s52, s58
	s_addc_u32 s53, s53, 0
	global_load_dwordx4 v[228:231], v236, s[52:53] nt
	global_load_dwordx4 v[232:235], v236, s[52:53] offset:16 nt
	s_waitcnt vmcnt(9)
	s_branch .Ls1_join
.Ls1_bl:
	s_mov_b32 s59, 7
	s_waitcnt vmcnt(16)
	v_cvt_pk_f16_f32 v228, v228, v229
	v_cvt_pk_f16_f32 v229, v230, v231
	v_cvt_pk_f16_f32 v230, v232, v233
	v_cvt_pk_f16_f32 v231, v234, v235
	s_cmp_lt_u32 s59, 4
	s_cselect_b32 s52, s62, s64
	s_cselect_b32 s53, s63, s65
	s_and_b32 s58, s59, 3
	s_lshl_b32 s58, s58, 15
	s_add_u32 s58, s58, 0x800
	s_add_u32 s52, s52, s58
	s_addc_u32 s53, s53, 0
	global_store_dwordx4 v237, v[228:231], s[52:53] sc1 nt
	s_waitcnt vmcnt(7)
	s_branch .Ls1_join

.Ls1_km:
	s_sub_u32 s59, s49, 19
	s_waitcnt vmcnt(16)
	v_cvt_pk_f16_f32 v228, v228, v229
	v_cvt_pk_f16_f32 v229, v230, v231
	v_cvt_pk_f16_f32 v230, v232, v233
	v_cvt_pk_f16_f32 v231, v234, v235
	s_lshl_b32 s58, s59, 13
	s_add_u32 s52, s44, s58
	s_addc_u32 s53, s45, 0
	global_store_dwordx4 v227, v[228:231], s[52:53] sc1 nt
	s_add_u32 s59, s59, 1
	s_lshl_b32 s58, s59, 14
	s_add_u32 s52, s46, s58
	s_addc_u32 s53, s47, 0
	global_load_dwordx4 v[228:231], v226, s[52:53] nt
	global_load_dwordx4 v[232:235], v226, s[52:53] offset:16 nt
	s_waitcnt vmcnt(9)
	s_branch .Ls1_join
.Ls1_kl:
	s_mov_b32 s59, 7
	s_waitcnt vmcnt(16)
	v_cvt_pk_f16_f32 v228, v228, v229
	v_cvt_pk_f16_f32 v229, v230, v231
	v_cvt_pk_f16_f32 v230, v232, v233
	v_cvt_pk_f16_f32 v231, v234, v235
	s_lshl_b32 s58, s59, 13
	s_add_u32 s52, s44, s58
	s_addc_u32 s53, s45, 0
	global_store_dwordx4 v227, v[228:231], s[52:53] sc1 nt
	s_waitcnt vmcnt(7)
	s_branch .Ls1_join
